# speedup vs baseline: 1.3214x; 1.0005x over previous
.Lfast0:
	v_cvt_pk_f16_f32 v180, v46, v47
	v_cvt_pk_f16_f32 v181, v48, v49
	v_mfma_f32_16x16x32_f16 v[6:9], a[0:3], v[224:227], v[6:9]
	v_and_b32_dpp v228, v62, v167 row_ror:8 row_mask:0xf bank_mask:0xf
	v_and_b32_dpp v229, v63, v167 row_ror:8 row_mask:0xf bank_mask:0xf
	v_mfma_f32_16x16x32_f16 v[10:13], a[32:35], v[224:227], v[10:13]
	v_and_b32_dpp v230, v64, v167 row_ror:8 row_mask:0xf bank_mask:0xf
	v_and_b32_dpp v231, v65, v167 row_ror:8 row_mask:0xf bank_mask:0xf
	v_mfma_f32_16x16x32_f16 v[14:17], a[64:67], v[224:227], v[14:17]
	v_cvt_pk_f16_f32 v182, v50, v51
	v_cvt_pk_f16_f32 v183, v52, v53
	v_mfma_f32_16x16x32_f16 v[18:21], a[96:99], v[224:227], v[18:21]
	v_cvt_pk_f16_f32 v218, v38, v39
	v_cvt_pk_f16_f32 v219, v40, v41
	v_mfma_f32_16x16x32_f16 v[22:25], a[128:131], v[224:227], v[22:25]
	s_waitcnt vmcnt(2)
	v_mfma_f32_16x16x32_f16 v[26:29], a[160:163], v[224:227], v[26:29]
	v_bitop3_b32 v168, v66, v67, s30 bitop3:0x7e
	v_bitop3_b32 v169, v68, v69, s30 bitop3:0x7e
	v_mfma_f32_16x16x32_f16 v[30:33], a[192:195], v[224:227], v[30:33]
	v_bitop3_b32 v168, v168, v169, s18 bitop3:0xa8
	v_cmp_ne_u32_e32 vcc, 0, v168
	v_mfma_f32_16x16x32_f16 v[34:37], a[224:227], v[224:227], v[34:37]
	v_and_b32_e32 v232, v66, v167
	v_and_b32_e32 v233, v67, v167
	v_mfma_f32_16x16x32_f16 v[6:9], a[4:7], v[228:231], v[6:9]
	v_and_b32_e32 v234, v68, v167
	v_and_b32_e32 v235, v69, v167
	v_mfma_f32_16x16x32_f16 v[10:13], a[36:39], v[228:231], v[10:13]
	v_and_b32_dpp v236, v66, v167 row_ror:8 row_mask:0xf bank_mask:0xf
	v_and_b32_dpp v237, v67, v167 row_ror:8 row_mask:0xf bank_mask:0xf
	v_mfma_f32_16x16x32_f16 v[14:17], a[68:71], v[228:231], v[14:17]
	v_and_b32_dpp v238, v68, v167 row_ror:8 row_mask:0xf bank_mask:0xf
	v_and_b32_dpp v239, v69, v167 row_ror:8 row_mask:0xf bank_mask:0xf
	v_mfma_f32_16x16x32_f16 v[18:21], a[100:103], v[228:231], v[18:21]
	v_cvt_pk_f16_f32 v220, v42, v43
	v_cvt_pk_f16_f32 v221, v44, v45
	v_mfma_f32_16x16x32_f16 v[22:25], a[132:135], v[228:231], v[22:25]
	v_mfma_f32_16x16x32_f16 v[26:29], a[164:167], v[228:231], v[26:29]
	v_mfma_f32_16x16x32_f16 v[30:33], a[196:199], v[228:231], v[30:33]
	v_mfma_f32_16x16x32_f16 v[34:37], a[228:231], v[228:231], v[34:37]
	s_cbranch_vccnz .Lrestart1
